# baseline (speedup 1.0000x reference)
_Z5k_csrPKjS0_PKfPjPfPDF16_P15HIP_vector_typeIjLj4EE:
	s_load_dwordx2 s[4:5], s[0:1], 0x0
	s_load_dwordx2 s[6:7], s[0:1], 0x10
	s_mul_i32 s3, s2, 0xc4
	v_lshrrev_b32_e32 v25, 4, v0
	v_add_u32_e32 v28, s3, v25
	v_and_b32_e32 v1, 15, v0
	v_min_i32_e32 v4, 0xc34f, v28
	v_add_u32_e32 v26, 64, v28
	v_lshlrev_b32_e32 v18, 4, v1
	v_mov_b32_e32 v19, 0
	v_ashrrev_i32_e32 v5, 31, v4
	v_min_i32_e32 v6, 0xc34f, v26
	s_waitcnt lgkmcnt(0)
	v_lshl_add_u64 v[2:3], s[6:7], 0, v[18:19]
	v_lshlrev_b64 v[4:5], 8, v[4:5]
	v_ashrrev_i32_e32 v7, 31, v6
	v_lshl_add_u64 v[4:5], v[2:3], 0, v[4:5]
	v_lshlrev_b64 v[6:7], 8, v[6:7]
	v_add_u32_e32 v24, 0x80, v28
	v_lshl_add_u64 v[6:7], v[2:3], 0, v[6:7]
	v_mov_b32_e32 v56, v4
	v_mov_b32_e32 v57, v5
	v_mov_b32_e32 v58, v6
	v_mov_b32_e32 v59, v7
	v_min_i32_e32 v4, 0xc34f, v24
	v_or_b32_e32 v32, 0xc00, v0
	v_ashrrev_i32_e32 v5, 31, v4
	v_lshrrev_b32_e32 v23, 4, v32
	v_lshlrev_b64 v[4:5], 8, v[4:5]
	v_add_u32_e32 v22, s3, v23
	v_lshl_add_u64 v[20:21], v[2:3], 0, v[4:5]
	v_min_i32_e32 v4, 0xc34f, v22
	v_ashrrev_i32_e32 v5, 31, v4
	v_lshlrev_b64 v[4:5], 8, v[4:5]
	v_lshrrev_b32_e32 v1, 3, v0
	v_lshl_add_u64 v[30:31], v[2:3], 0, v[4:5]
	v_mov_b32_e32 v60, v20
	v_mov_b32_e32 v61, v21
	v_mov_b32_e32 v62, v30
	v_mov_b32_e32 v63, v31
	v_min_u32_e32 v20, 0x7c, v1
	s_mul_i32 s6, s2, 0x7d
	v_add_u32_e32 v30, s6, v20
	v_ashrrev_i32_e32 v31, 31, v30
	v_lshl_add_u64 v[30:31], v[30:31], 2, s[4:5]
	global_load_dword v21, v[30:31], off
	global_load_dword v27, v[30:31], off offset:500
	v_cmp_gt_u32_e32 vcc, 2, v0
	v_lshlrev_b32_e32 v1, 2, v0
	s_and_saveexec_b64 s[4:5], vcc
	v_lshlrev_b32_e32 v18, 2, v0
	ds_write_b32 v18, v19 offset:22528
	s_or_b64 exec, exec, s[4:5]
	s_movk_i32 s4, 0x100
	v_cmp_gt_u32_e64 s[8:9], s4, v0
	s_and_saveexec_b64 s[4:5], s[8:9]
	s_cbranch_execz .LBB1_4
	s_mov_b32 s6, 0x539782a
	v_mul_hi_u32 v29, v0, s6
	s_movk_i32 s6, 0xffcf
	v_lshlrev_b32_e32 v18, 2, v0
	v_mov_b32_e32 v19, 0
	v_mad_i32_i24 v29, v29, s6, v0
	ds_write2st64_b32 v18, v19, v29 offset0:64 offset1:72

.LBB1_13:
	s_or_b64 exec, exec, s[6:7]
	s_load_dwordx2 s[34:35], s[0:1], 0x28
	s_movk_i32 s0, 0x1400
	v_mad_u32_u24 v27, v20, s0, v21
	v_add_u32_e32 v20, v18, v27
	v_min_u32_e32 v20, 0x9c3ff, v20
	v_or_b32_e32 v31, 8, v18
	v_lshlrev_b32_e32 v29, 2, v20
	v_add_u32_e32 v20, v31, v27
	v_min_u32_e32 v20, 0x9c3ff, v20
	v_or_b32_e32 v30, 16, v18
	v_lshlrev_b32_e32 v35, 2, v20
	v_add_u32_e32 v20, v30, v27
	v_min_u32_e32 v20, 0x9c3ff, v20
	v_lshlrev_b32_e32 v36, 2, v20
	v_or_b32_e32 v20, 24, v18
	v_add_u32_e32 v21, v20, v27
	v_min_u32_e32 v21, 0x9c3ff, v21
	v_lshlrev_b32_e32 v37, 2, v21
	global_load_dword v38, v29, s[26:27]
	global_load_dword v34, v35, s[26:27]
	global_load_dword v33, v36, s[26:27]
	global_load_dword v21, v37, s[26:27]
	global_load_dwordx4 v[14:17], v[56:57], off nt
	global_load_dwordx4 v[10:13], v[58:59], off nt
	global_load_dwordx4 v[6:9], v[60:61], off nt
	global_load_dwordx4 v[2:5], v[62:63], off nt
	v_cndmask_b32_e32 v29, 0, v19, vcc
	v_cmp_lt_u32_e32 vcc, v18, v29
	s_waitcnt vmcnt(7)
	s_nop 0
	v_cndmask_b32_e32 v37, -1, v38, vcc
	v_cmp_ne_u32_e64 s[6:7], -1, v37
	s_and_saveexec_b64 s[0:1], s[6:7]
	v_mov_b32_e32 v19, 2
	v_lshlrev_b32_sdwa v19, v19, v37 dst_sel:DWORD dst_unused:UNUSED_PAD src0_sel:DWORD src1_sel:WORD_1
	v_mov_b32_e32 v35, 1
	ds_add_u32 v19, v35 offset:16384
	s_or_b64 exec, exec, s[0:1]
	v_cmp_lt_u32_e32 vcc, v31, v29
	s_waitcnt vmcnt(6)
	s_nop 0
	v_cndmask_b32_e32 v36, -1, v34, vcc
	v_cmp_ne_u32_e64 s[4:5], -1, v36
	s_and_saveexec_b64 s[0:1], s[4:5]
	v_mov_b32_e32 v19, 2
	v_lshlrev_b32_sdwa v19, v19, v36 dst_sel:DWORD dst_unused:UNUSED_PAD src0_sel:DWORD src1_sel:WORD_1
	v_mov_b32_e32 v31, 1
	ds_add_u32 v19, v31 offset:16384
	s_or_b64 exec, exec, s[0:1]
	v_cmp_lt_u32_e32 vcc, v30, v29
	s_waitcnt vmcnt(5)
	s_nop 0
	v_cndmask_b32_e32 v35, -1, v33, vcc
	v_cmp_ne_u32_e64 s[16:17], -1, v35
	s_and_saveexec_b64 s[0:1], s[16:17]
	v_mov_b32_e32 v19, 2
	v_lshlrev_b32_sdwa v19, v19, v35 dst_sel:DWORD dst_unused:UNUSED_PAD src0_sel:DWORD src1_sel:WORD_1
	v_mov_b32_e32 v30, 1
	ds_add_u32 v19, v30 offset:16384
	s_or_b64 exec, exec, s[0:1]
	v_cmp_lt_u32_e32 vcc, v20, v29
	s_waitcnt vmcnt(4)
	s_nop 0
	v_cndmask_b32_e32 v34, -1, v21, vcc
	v_cmp_ne_u32_e64 s[0:1], -1, v34
	s_and_saveexec_b64 s[10:11], s[0:1]
	v_mov_b32_e32 v19, 2
	v_lshlrev_b32_sdwa v19, v19, v34 dst_sel:DWORD dst_unused:UNUSED_PAD src0_sel:DWORD src1_sel:WORD_1
	v_mov_b32_e32 v20, 1
	ds_add_u32 v19, v20 offset:16384
	s_or_b64 exec, exec, s[10:11]
	v_or_b32_e32 v33, 32, v18
	v_cmp_lt_u32_e32 vcc, v33, v29
	s_and_saveexec_b64 s[12:13], vcc
	s_cbranch_execz .LBB1_24
	s_mov_b64 s[14:15], 0
	v_mov_b32_e32 v19, 0
	v_mov_b32_e32 v20, 1
	v_mov_b32_e32 v21, 2
	v_mov_b32_e32 v30, v33

.LBB1_65:
	s_or_b64 exec, exec, s[0:1]
	s_mov_b32 s40, 0xc350
	s_movk_i32 s41, 0xc40
	s_waitcnt vmcnt(0)
	v_lshlrev_b32_e32 v48, 3, v0
	v_and_b32_e32 v48, 0x78, v48
	v_mov_b32_e32 v49, 0
	v_lshl_add_u64 v[48:49], s[34:35], 0, v[48:49]
	v_lshlrev_b32_e32 v50, 2, v25
	v_cmp_gt_i32_e64 s[44:45], s40, v28
	s_and_saveexec_b64 s[42:43], s[44:45]
	ds_read_b32 v51, v50 offset:19456
	v_mov_b32_e32 v52, v28
	v_mov_b32_e32 v53, 0
	v_lshlrev_b64 v[52:53], 7, v[52:53]
	s_waitcnt lgkmcnt(0)
	v_mul_f32_e32 v14, v51, v14
	v_mul_f32_e32 v15, v51, v15
	v_mul_f32_e32 v16, v51, v16
	v_mul_f32_e32 v17, v51, v17
	v_cvt_pk_f16_f32 v14, v14, v15
	v_cvt_pk_f16_f32 v15, v16, v17
	v_lshl_add_u64 v[52:53], v[48:49], 0, v[52:53]
	global_store_dwordx2 v[52:53], v[14:15], off sc0 sc1
	s_or_b64 exec, exec, s[42:43]
	v_cmp_gt_i32_e64 s[44:45], s40, v26
	s_and_saveexec_b64 s[42:43], s[44:45]
	ds_read_b32 v51, v50 offset:19712
	v_mov_b32_e32 v52, v26
	v_mov_b32_e32 v53, 0
	v_lshlrev_b64 v[52:53], 7, v[52:53]
	s_waitcnt lgkmcnt(0)
	v_mul_f32_e32 v10, v51, v10
	v_mul_f32_e32 v11, v51, v11
	v_mul_f32_e32 v12, v51, v12
	v_mul_f32_e32 v13, v51, v13
	v_cvt_pk_f16_f32 v10, v10, v11
	v_cvt_pk_f16_f32 v11, v12, v13
	v_lshl_add_u64 v[52:53], v[48:49], 0, v[52:53]
	global_store_dwordx2 v[52:53], v[10:11], off sc0 sc1
	s_or_b64 exec, exec, s[42:43]
	v_cmp_gt_i32_e64 s[44:45], s40, v24
	s_and_saveexec_b64 s[42:43], s[44:45]
	ds_read_b32 v51, v50 offset:19968
	v_mov_b32_e32 v52, v24
	v_mov_b32_e32 v53, 0
	v_lshlrev_b64 v[52:53], 7, v[52:53]
	s_waitcnt lgkmcnt(0)
	v_mul_f32_e32 v6, v51, v6
	v_mul_f32_e32 v7, v51, v7
	v_mul_f32_e32 v8, v51, v8
	v_mul_f32_e32 v9, v51, v9
	v_cvt_pk_f16_f32 v6, v6, v7
	v_cvt_pk_f16_f32 v7, v8, v9
	v_lshl_add_u64 v[52:53], v[48:49], 0, v[52:53]
	global_store_dwordx2 v[52:53], v[6:7], off sc0 sc1
	s_or_b64 exec, exec, s[42:43]
	v_cmp_gt_u32_e64 s[44:45], s41, v32
	v_cmp_gt_i32_e64 s[46:47], s40, v22
	s_and_b64 s[44:45], s[44:45], s[46:47]
	v_lshlrev_b32_e32 v54, 2, v23
	s_and_saveexec_b64 s[42:43], s[44:45]
	ds_read_b32 v51, v54 offset:19456
	v_mov_b32_e32 v52, v22
	v_mov_b32_e32 v53, 0
	v_lshlrev_b64 v[52:53], 7, v[52:53]
	s_waitcnt lgkmcnt(0)
	v_mul_f32_e32 v2, v51, v2
	v_mul_f32_e32 v3, v51, v3
	v_mul_f32_e32 v4, v51, v4
	v_mul_f32_e32 v5, v51, v5
	v_cvt_pk_f16_f32 v2, v2, v3
	v_cvt_pk_f16_f32 v3, v4, v5
	v_lshl_add_u64 v[52:53], v[48:49], 0, v[52:53]
	global_store_dwordx2 v[52:53], v[2:3], off sc0 sc1
	s_or_b64 exec, exec, s[42:43]
	v_cmp_le_u32_e32 vcc, v31, v0
	s_waitcnt lgkmcnt(0)
	s_barrier
	s_and_saveexec_b64 s[0:1], vcc
	s_xor_b64 s[0:1], exec, s[0:1]
	v_lshlrev_b32_e32 v1, 2, v0
	s_andn2_saveexec_b64 s[0:1], s[0:1]
	s_cbranch_execz .LBB1_71
	v_min_u32_e32 v20, 0x1000, v31
	s_mov_b64 s[2:3], 0
	v_mov_b32_e32 v19, 0
	v_mov_b32_e32 v21, v1

	.amdhsa_kernel _Z5k_csrPKjS0_PKfPjPfPDF16_P15HIP_vector_typeIjLj4EE
		.amdhsa_group_segment_fixed_size 22536
		.amdhsa_private_segment_fixed_size 0
		.amdhsa_kernarg_size 56
		.amdhsa_user_sgpr_count 2
		.amdhsa_user_sgpr_dispatch_ptr 0
		.amdhsa_user_sgpr_queue_ptr 0
		.amdhsa_user_sgpr_kernarg_segment_ptr 1
		.amdhsa_user_sgpr_dispatch_id 0
		.amdhsa_user_sgpr_kernarg_preload_length 0
		.amdhsa_user_sgpr_kernarg_preload_offset 0
		.amdhsa_user_sgpr_private_segment_size 0
		.amdhsa_uses_dynamic_stack 0
		.amdhsa_enable_private_segment 0
		.amdhsa_system_sgpr_workgroup_id_x 1
		.amdhsa_system_sgpr_workgroup_id_y 0
		.amdhsa_system_sgpr_workgroup_id_z 0
		.amdhsa_system_sgpr_workgroup_info 0
		.amdhsa_system_vgpr_workitem_id 0
		.amdhsa_next_free_vgpr 64
		.amdhsa_next_free_sgpr 48
		.amdhsa_accum_offset 64
		.amdhsa_reserve_vcc 1
		.amdhsa_float_round_mode_32 0
		.amdhsa_float_round_mode_16_64 0
		.amdhsa_float_denorm_mode_32 3
		.amdhsa_float_denorm_mode_16_64 3
		.amdhsa_dx10_clamp 1
		.amdhsa_ieee_mode 1
		.amdhsa_fp16_overflow 0
		.amdhsa_tg_split 0
		.amdhsa_exception_fp_ieee_invalid_op 0
		.amdhsa_exception_fp_denorm_src 0
		.amdhsa_exception_fp_ieee_div_zero 0
		.amdhsa_exception_fp_ieee_overflow 0
		.amdhsa_exception_fp_ieee_underflow 0
		.amdhsa_exception_fp_ieee_inexact 0
		.amdhsa_exception_int_div_zero 0
	.end_amdhsa_kernel

amdhsa.kernels:
  - .agpr_count:     0
    .args:
      - .actual_access:  read_only
        .address_space:  global
        .offset:         0
        .size:           8
        .value_kind:     global_buffer
      - .actual_access:  read_only
        .address_space:  global
        .offset:         8
        .size:           8
        .value_kind:     global_buffer
      - .actual_access:  write_only
        .address_space:  global
        .offset:         16
        .size:           8
        .value_kind:     global_buffer
      - .actual_access:  write_only
        .address_space:  global
        .offset:         24
        .size:           8
        .value_kind:     global_buffer
      - .actual_access:  read_only
        .address_space:  global
        .offset:         32
        .size:           8
        .value_kind:     global_buffer
      - .actual_access:  read_only
        .address_space:  global
        .offset:         40
        .size:           8
        .value_kind:     global_buffer
      - .actual_access:  read_only
        .address_space:  global
        .offset:         48
        .size:           8
        .value_kind:     global_buffer
      - .actual_access:  read_only
        .address_space:  global
        .offset:         56
        .size:           8
        .value_kind:     global_buffer
      - .actual_access:  read_only
        .address_space:  global
        .offset:         64
        .size:           8
        .value_kind:     global_buffer
      - .actual_access:  write_only
        .address_space:  global
        .offset:         72
        .size:           8
        .value_kind:     global_buffer
      - .actual_access:  write_only
        .address_space:  global
        .offset:         80
        .size:           8
        .value_kind:     global_buffer
      - .actual_access:  write_only
        .address_space:  global
        .offset:         88
        .size:           8
        .value_kind:     global_buffer
      - .actual_access:  write_only
        .address_space:  global
        .offset:         96
        .size:           8
        .value_kind:     global_buffer
      - .actual_access:  write_only
        .address_space:  global
        .offset:         104
        .size:           8
        .value_kind:     global_buffer
      - .actual_access:  write_only
        .address_space:  global
        .offset:         112
        .size:           8
        .value_kind:     global_buffer
      - .offset:         120
        .size:           4
        .value_kind:     hidden_block_count_x
      - .offset:         124
        .size:           4
        .value_kind:     hidden_block_count_y
      - .offset:         128
        .size:           4
        .value_kind:     hidden_block_count_z
      - .offset:         132
        .size:           2
        .value_kind:     hidden_group_size_x
      - .offset:         134
        .size:           2
        .value_kind:     hidden_group_size_y
      - .offset:         136
        .size:           2
        .value_kind:     hidden_group_size_z
      - .offset:         138
        .size:           2
        .value_kind:     hidden_remainder_x
      - .offset:         140
        .size:           2
        .value_kind:     hidden_remainder_y
      - .offset:         142
        .size:           2
        .value_kind:     hidden_remainder_z
      - .offset:         160
        .size:           8
        .value_kind:     hidden_global_offset_x
      - .offset:         168
        .size:           8
        .value_kind:     hidden_global_offset_y
      - .offset:         176
        .size:           8
        .value_kind:     hidden_global_offset_z
      - .offset:         184
        .size:           2
        .value_kind:     hidden_grid_dims
    .group_segment_fixed_size: 21520
    .kernarg_segment_align: 8
    .kernarg_segment_size: 376
    .language:       OpenCL C
    .language_version:
      - 2
      - 0
    .max_flat_workgroup_size: 1024
    .name:           _Z11k_chunksortPKiS0_PjS1_PKfS3_S3_S3_S3_PDF16_S4_PfS5_S4_Ph
    .private_segment_fixed_size: 0
    .sgpr_count:     32
    .sgpr_spill_count: 0
    .symbol:         _Z11k_chunksortPKiS0_PjS1_PKfS3_S3_S3_S3_PDF16_S4_PfS5_S4_Ph.kd
    .uniform_work_group_size: 1
    .uses_dynamic_stack: false
    .vgpr_count:     38
    .vgpr_spill_count: 0
    .wavefront_size: 64
  - .agpr_count:     0
    .args:
      - .actual_access:  read_only
        .address_space:  global
        .offset:         0
        .size:           8
        .value_kind:     global_buffer
      - .actual_access:  read_only
        .address_space:  global
        .offset:         8
        .size:           8
        .value_kind:     global_buffer
      - .actual_access:  read_only
        .address_space:  global
        .offset:         16
        .size:           8
        .value_kind:     global_buffer
      - .actual_access:  write_only
        .address_space:  global
        .offset:         24
        .size:           8
        .value_kind:     global_buffer
      - .actual_access:  write_only
        .address_space:  global
        .offset:         32
        .size:           8
        .value_kind:     global_buffer
      - .actual_access:  write_only
        .address_space:  global
        .offset:         40
        .size:           8
        .value_kind:     global_buffer
      - .actual_access:  write_only
        .address_space:  global
        .offset:         48
        .size:           8
        .value_kind:     global_buffer
    .group_segment_fixed_size: 22536
    .kernarg_segment_align: 8
    .kernarg_segment_size: 56
    .language:       OpenCL C
    .language_version:
      - 2
      - 0
    .max_flat_workgroup_size: 1024
    .name:           _Z5k_csrPKjS0_PKfPjPfPDF16_P15HIP_vector_typeIjLj4EE
    .private_segment_fixed_size: 0
    .sgpr_count:     54
    .sgpr_spill_count: 0
    .symbol:         _Z5k_csrPKjS0_PKfPjPfPDF16_P15HIP_vector_typeIjLj4EE.kd
    .uniform_work_group_size: 1
    .uses_dynamic_stack: false
    .vgpr_count:     64
    .vgpr_spill_count: 0
    .wavefront_size: 64
  - .agpr_count:     0
    .args:
      - .actual_access:  read_only
        .address_space:  global
        .offset:         0
        .size:           8
        .value_kind:     global_buffer
      - .actual_access:  read_only
        .address_space:  global
        .offset:         8
        .size:           8
        .value_kind:     global_buffer
      - .actual_access:  read_only
        .address_space:  global
        .offset:         16
        .size:           8
        .value_kind:     global_buffer
      - .actual_access:  read_only
        .address_space:  global
        .offset:         24
        .size:           8
        .value_kind:     global_buffer
      - .actual_access:  read_only
        .address_space:  global
        .offset:         32
        .size:           8
        .value_kind:     global_buffer
      - .actual_access:  read_only
        .address_space:  global
        .offset:         40
        .size:           8
        .value_kind:     global_buffer
      - .actual_access:  read_only
        .address_space:  global
        .offset:         48
        .size:           8
        .value_kind:     global_buffer
      - .actual_access:  write_only
        .address_space:  global
        .offset:         56
        .size:           8
        .value_kind:     global_buffer
      - .actual_access:  write_only
        .address_space:  global
        .offset:         64
        .size:           8
        .value_kind:     global_buffer
    .group_segment_fixed_size: 36112
    .kernarg_segment_align: 8
    .kernarg_segment_size: 72
    .language:       OpenCL C
    .language_version:
      - 2
      - 0
    .max_flat_workgroup_size: 256
    .name:           _Z8k_layer1PKfPKDF16_PK15HIP_vector_typeIjLj4EEPKjS0_S2_S0_PhPf
    .private_segment_fixed_size: 0
    .sgpr_count:     30
    .sgpr_spill_count: 0
    .symbol:         _Z8k_layer1PKfPKDF16_PK15HIP_vector_typeIjLj4EEPKjS0_S2_S0_PhPf.kd
    .uniform_work_group_size: 1
    .uses_dynamic_stack: false
    .vgpr_count:     128
    .vgpr_spill_count: 0
    .wavefront_size: 64
  - .agpr_count:     0
    .args:
      - .actual_access:  read_only
        .address_space:  global
        .offset:         0
        .size:           8
        .value_kind:     global_buffer
      - .actual_access:  read_only
        .address_space:  global
        .offset:         8
        .size:           8
        .value_kind:     global_buffer
      - .actual_access:  read_only
        .address_space:  global
        .offset:         16
        .size:           8
        .value_kind:     global_buffer
      - .actual_access:  read_only
        .address_space:  global
        .offset:         24
        .size:           8
        .value_kind:     global_buffer
      - .actual_access:  read_only
        .address_space:  global
        .offset:         32
        .size:           8
        .value_kind:     global_buffer
      - .actual_access:  read_only
        .address_space:  global
        .offset:         40
        .size:           8
        .value_kind:     global_buffer
      - .actual_access:  read_only
        .address_space:  global
        .offset:         48
        .size:           8
        .value_kind:     global_buffer
      - .address_space:  global
        .offset:         56
        .size:           8
        .value_kind:     global_buffer
    .group_segment_fixed_size: 39168
    .kernarg_segment_align: 8
    .kernarg_segment_size: 64
    .language:       OpenCL C
    .language_version:
      - 2
      - 0
    .max_flat_workgroup_size: 256
    .name:           _Z8k_layer2PKhPKfPK15HIP_vector_typeIjLj4EEPKjS2_PKDF16_S2_Pf
    .private_segment_fixed_size: 0
    .sgpr_count:     27
    .sgpr_spill_count: 0
    .symbol:         _Z8k_layer2PKhPKfPK15HIP_vector_typeIjLj4EEPKjS2_PKDF16_S2_Pf.kd
    .uniform_work_group_size: 1
    .uses_dynamic_stack: false
    .vgpr_count:     128
    .vgpr_spill_count: 0
    .wavefront_size: 64
  - .agpr_count:     0
    .args:
      - .actual_access:  read_only
        .address_space:  global
        .offset:         0
        .size:           8
        .value_kind:     global_buffer
      - .actual_access:  read_only
        .address_space:  global
        .offset:         8
        .size:           8
        .value_kind:     global_buffer
      - .actual_access:  read_only
        .address_space:  global
        .offset:         16
        .size:           8
        .value_kind:     global_buffer
      - .actual_access:  read_only
        .address_space:  global
        .offset:         24
        .size:           8
        .value_kind:     global_buffer
      - .actual_access:  read_only
        .address_space:  global
        .offset:         32
        .size:           8
        .value_kind:     global_buffer
      - .actual_access:  write_only
        .address_space:  global
        .offset:         40
        .size:           8
        .value_kind:     global_buffer
    .group_segment_fixed_size: 512
    .kernarg_segment_align: 8
    .kernarg_segment_size: 48
    .language:       OpenCL C
    .language_version:
      - 2
      - 0
    .max_flat_workgroup_size: 320
    .name:           _Z7k_headsPKfS0_S0_S0_S0_Pf
    .private_segment_fixed_size: 0
    .sgpr_count:     22
    .sgpr_spill_count: 0
    .symbol:         _Z7k_headsPKfS0_S0_S0_S0_Pf.kd
    .uniform_work_group_size: 1
    .uses_dynamic_stack: false
    .vgpr_count:     56
    .vgpr_spill_count: 0
    .wavefront_size: 64
